# speedup vs baseline: 1.0278x; 1.0278x over previous
.Lco_nopoll:
	s_waitcnt lgkmcnt(0)
	s_barrier
	v_mov_b32_e32 v76, 0
	v_mov_b32_e32 v77, 0
	v_mov_b32_e32 v78, 0
	v_mov_b32_e32 v79, 0
	ds_write_b128 v74, v[76:79]
	ds_write_b128 v74, v[76:79] offset:8192
	ds_write_b128 v74, v[76:79] offset:16384
	ds_write_b128 v74, v[76:79] offset:24576
	ds_write_b128 v74, v[76:79] offset:32768
	ds_write_b128 v74, v[76:79] offset:40960
	ds_write_b128 v74, v[76:79] offset:49152
	ds_write_b128 v74, v[76:79] offset:57344
	v_mov_b32_e32 v0, 0x26400
	v_lshl_add_u32 v0, v75, 5, v0
	ds_read_b128 v[36:39], v0
	ds_read_b128 v[40:43], v0 offset:16
	s_waitcnt lgkmcnt(0)
	v_or3_b32 v44, v36, v37, v38
	v_or3_b32 v44, v44, v39, v40
	v_or3_b32 v44, v44, v41, v42
	v_or_b32_e32 v44, v44, v43
	v_bfe_u32 v44, v44, 15, 1
	v_and_b32_e32 v36, 0x7f, v36
	v_and_b32_e32 v37, 0x7f, v37
	v_and_b32_e32 v38, 0x7f, v38
	v_and_b32_e32 v39, 0x7f, v39
	v_and_b32_e32 v40, 0x7f, v40
	v_and_b32_e32 v41, 0x7f, v41
	v_and_b32_e32 v42, 0x7f, v42
	v_and_b32_e32 v43, 0x7f, v43
	v_mov_b32_e32 v45, v36
	v_add_u32_e32 v46, v45, v37
	v_add_u32_e32 v47, v46, v38
	v_add_u32_e32 v48, v47, v39
	v_add_u32_e32 v49, v48, v40
	v_add_u32_e32 v50, v49, v41
	v_add_u32_e32 v51, v50, v42
	v_add_u32_e32 v52, v51, v43
	v_cmp_lt_u32_e32 vcc, 0x100, v52
	v_add_u32_e32 v53, 15, v52
	v_lshrrev_b32_e32 v53, 4, v53
	v_cndmask_b32_e64 v54, 0, 1, vcc
	v_or_b32_e32 v44, v44, v54
	v_mov_b32_e32 v55, 0x26c00
	v_cmp_eq_u32_e32 vcc, 0, v70
	s_and_saveexec_b64 s[14:15], vcc
	ds_max_u32 v55, v53
	ds_or_b32 v55, v44 offset:4
	s_mov_b64 exec, s[14:15]
	s_waitcnt lgkmcnt(0)
	s_barrier
	ds_read_b64 v[0:1], v55
	v_lshlrev_b32_e32 v56, 5, v45
	v_lshlrev_b32_e32 v57, 5, v46
	v_lshlrev_b32_e32 v58, 5, v47
	v_lshlrev_b32_e32 v59, 5, v48
	v_lshlrev_b32_e32 v60, 5, v49
	v_lshlrev_b32_e32 v61, 5, v50
	v_lshlrev_b32_e32 v62, 5, v51
	v_sub_u32_e32 v56, 0x800, v56
	v_sub_u32_e32 v57, 0x1000, v57
	v_sub_u32_e32 v58, 0x1800, v58
	v_sub_u32_e32 v59, 0x2000, v59
	v_sub_u32_e32 v60, 0x2800, v60
	v_sub_u32_e32 v61, 0x3000, v61
	v_sub_u32_e32 v62, 0x3800, v62
	v_add_u32_e32 v63, s3, v75
	v_lshlrev_b32_e32 v63, 14, v63
	v_add_u32_e32 v63, 0x800000, v63
	s_waitcnt lgkmcnt(0)
	v_readfirstlane_b32 s77, v0
	v_readfirstlane_b32 s36, v1
	s_add_i32 s77, s77, 0
	s_cmp_lg_u32 s36, 0
	s_cselect_b64 s[6:7], 0, -1
	s_cmp_gt_u32 s10, 3
	s_cbranch_scc1 .Lco_done
	s_cmp_lg_u32 s36, 0
	s_cbranch_scc1 .Lco_gen
	s_mov_b32 s89, 0
